# z_setup: norm-weight load issued together with the conv-tap loads (one wait instead of two); on top of SWA V/Q prefetch
# speedup vs baseline: 1.0046x; 1.0046x over previous
; #define LAS __attribute__((address_space(3)))
; __device__ __forceinline__ void prefetch(Pre& P, const bf16_t* proj, const float* gates, size_t rb, int c, int h, int tid, int lane) {
;     const int cc = tid & 31, rg = tid >> 5;
;     const int col = (cc < 16) ? (C_LQ + h * 128 + 8 * cc) : (C_LK + h * 128 + 8 * (cc - 16));
; #pragma unroll
;     for (int i = 0; i < 7; ++i) { const int pos = c * 64 + 4 * rg - 3 + i;
;         if (pos >= 0) P.raw[i] = *(const u32x4*)(proj + (rb + pos) * NIN + col); else P.raw[i] = (u32x4){0u, 0u, 0u, 0u}; }
; __device__ __forceinline__ void z_setup(Frame& F, const float* conv_w, const float* conv_b, const float* normw) {
;     __syncthreads();
;     for (int i = F.tid; i < 5 * 1024; i += NTHR) { const int j = i >> 10, ch = i & 1023; ((LAS float*)(F.lds + ZCW))[i] = (j < 4) ? conv_w[j * 1024 + ch] : conv_b[ch]; }
;     ((LAS float*)(F.lds + ZNW))[F.tid] = normw[F.tid];
;     __syncthreads();
; }
.LBB0_645:
	s_mov_b64 s[8:9], 0x1000
	v_lshl_add_u64 v[10:11], v[4:5], 0, s[8:9]
	v_lshl_add_u64 v[12:13], v[10:11], 0, s[8:9]
	v_lshl_add_u64 v[14:15], v[12:13], 0, s[8:9]
	v_lshl_add_u64 v[16:17], s[6:7], 0, v[2:3]
	global_load_dword v20, v[4:5], off
	global_load_dword v21, v[4:5], off offset:2048
	global_load_dword v22, v[10:11], off
	global_load_dword v23, v[10:11], off offset:2048
	global_load_dword v24, v[12:13], off
	global_load_dword v25, v[12:13], off offset:2048
	global_load_dword v26, v[14:15], off
	global_load_dword v27, v[14:15], off offset:2048
	global_load_dword v28, v[16:17], off
	global_load_dword v29, v[16:17], off offset:2048
	v_mov_b32_e32 v34, 0
	v_lshlrev_b32_e32 v110, 2, v0
	v_mov_b32_e32 v111, v34
	v_lshl_add_u64 v[2:3], s[0:1], 0, v[110:111]
	global_load_dword v30, v[2:3], off
	s_waitcnt vmcnt(0)
	ds_write_b32 v1, v20
	ds_write_b32 v1, v21 offset:2048
	ds_write_b32 v1, v22 offset:4096
	ds_write_b32 v1, v23 offset:6144
	ds_write_b32 v1, v24 offset:8192
	ds_write_b32 v1, v25 offset:10240
	ds_write_b32 v1, v26 offset:12288
	ds_write_b32 v1, v27 offset:14336
	ds_write_b32 v1, v28 offset:16384
	ds_write_b32 v1, v29 offset:18432
	v_lshl_add_u32 v2, v0, 2, 0
	s_cmpk_lt_i32 s2, 0x400
	v_add_u32_e32 v2, 0x1f300, v2
	s_cselect_b64 s[0:1], -1, 0
	s_cmpk_gt_i32 s2, 0x3ff
	s_waitcnt lgkmcnt(0)
	ds_write_b32 v2, v30
	s_waitcnt lgkmcnt(0)
	s_barrier
	s_cbranch_scc1 .LBB0_656
	s_ashr_i32 s3, s2, 5
	s_and_b32 s4, s3, 3
	v_and_b32_e32 v1, 31, v0
	s_lshl_b32 s11, s4, 7
	v_lshlrev_b32_e32 v2, 3, v1
	v_or_b32_e32 v3, s11, v2
	v_add_u32_e32 v2, s11, v2
	s_lshl_b32 s8, s2, 6
	v_or_b32_e32 v3, 0x600, v3
	v_add_u32_e32 v2, 0x780, v2
	v_cmp_gt_u32_e32 vcc, 16, v1
	s_ashr_i32 s6, s2, 7
	s_and_b32 s10, s8, 0x7c0
	v_lshrrev_b32_e32 v8, 5, v0
	v_cndmask_b32_e32 v3, v2, v3, vcc
	s_ashr_i32 s7, s6, 31
	v_lshl_or_b32 v2, v8, 2, s10
	v_lshlrev_b32_e32 v4, 1, v3
	v_mov_b32_e32 v5, v34
	s_lshl_b64 s[6:7], s[6:7], 11
	v_add_u32_e32 v6, -3, v2
	v_lshl_add_u64 v[4:5], s[58:59], 0, v[4:5]
	v_cmp_ne_u32_e32 vcc, 0, v2
	v_mov_b32_e32 v35, 0
	v_mov_b32_e32 v36, 0
	v_mov_b32_e32 v37, 0
	s_and_saveexec_b64 s[8:9], vcc
	s_cbranch_execz .LBB0_649
	v_mov_b32_e32 v7, 0
	v_lshl_add_u64 v[10:11], s[6:7], 0, v[6:7]
	s_movk_i32 s14, 0x2600
	v_mad_u64_u32 v[12:13], s[12:13], v10, s14, v[4:5]
	v_mad_i32_i24 v13, v11, s14, v13
	global_load_dwordx4 v[34:37], v[12:13], off

; #define LAS __attribute__((address_space(3)))
; __device__ __forceinline__ void prefetch(Pre& P, const bf16_t* proj, const float* gates, size_t rb, int c, int h, int tid, int lane) {
;     const int cc = tid & 31, rg = tid >> 5;
;     const int col = (cc < 16) ? (C_LQ + h * 128 + 8 * cc) : (C_LK + h * 128 + 8 * (cc - 16));
; #pragma unroll
;     for (int i = 0; i < 7; ++i) { const int pos = c * 64 + 4 * rg - 3 + i;
;         if (pos >= 0) P.raw[i] = *(const u32x4*)(proj + (rb + pos) * NIN + col); else P.raw[i] = (u32x4){0u, 0u, 0u, 0u}; }
; __device__ __forceinline__ void z_setup(Frame& F, const float* conv_w, const float* conv_b, const float* normw) {
;     __syncthreads();
;     for (int i = F.tid; i < 5 * 1024; i += NTHR) { const int j = i >> 10, ch = i & 1023; ((LAS float*)(F.lds + ZCW))[i] = (j < 4) ? conv_w[j * 1024 + ch] : conv_b[ch]; }
;     ((LAS float*)(F.lds + ZNW))[F.tid] = normw[F.tid];
;     __syncthreads();
; }
.LBB0_1773:
	s_mov_b64 s[8:9], 0x1000
	v_lshl_add_u64 v[10:11], v[4:5], 0, s[8:9]
	v_lshl_add_u64 v[12:13], v[10:11], 0, s[8:9]
	v_lshl_add_u64 v[14:15], v[12:13], 0, s[8:9]
	v_lshl_add_u64 v[16:17], s[0:1], 0, v[2:3]
	global_load_dword v20, v[4:5], off
	global_load_dword v21, v[4:5], off offset:2048
	global_load_dword v22, v[10:11], off
	global_load_dword v23, v[10:11], off offset:2048
	global_load_dword v24, v[12:13], off
	global_load_dword v25, v[12:13], off offset:2048
	global_load_dword v26, v[14:15], off
	global_load_dword v27, v[14:15], off offset:2048
	global_load_dword v28, v[16:17], off
	global_load_dword v29, v[16:17], off offset:2048
	v_mov_b32_e32 v34, 0
	v_lshlrev_b32_e32 v110, 2, v0
	v_mov_b32_e32 v111, v34
	v_lshl_add_u64 v[2:3], s[6:7], 0, v[110:111]
	global_load_dword v30, v[2:3], off offset:2048
	s_waitcnt vmcnt(0)
	ds_write_b32 v1, v20
	ds_write_b32 v1, v21 offset:2048
	ds_write_b32 v1, v22 offset:4096
	ds_write_b32 v1, v23 offset:6144
	ds_write_b32 v1, v24 offset:8192
	ds_write_b32 v1, v25 offset:10240
	ds_write_b32 v1, v26 offset:12288
	ds_write_b32 v1, v27 offset:14336
	ds_write_b32 v1, v28 offset:16384
	ds_write_b32 v1, v29 offset:18432
	v_lshl_add_u32 v2, v0, 2, 0
	s_cmpk_lt_i32 s2, 0x400
	v_add_u32_e32 v2, 0x1f300, v2
	s_cselect_b64 s[0:1], -1, 0
	s_cmpk_gt_i32 s2, 0x3ff
	s_waitcnt lgkmcnt(0)
	ds_write_b32 v2, v30
	s_waitcnt lgkmcnt(0)
	s_barrier
	s_cbranch_scc1 .LBB0_1784
	s_ashr_i32 s3, s2, 5
	s_and_b32 s4, s3, 3
	s_lshl_b32 s11, s4, 7
	v_lshlrev_b32_e32 v2, 3, v203
	v_or_b32_e32 v3, s11, v2
	v_add_u32_e32 v2, s11, v2
	s_lshl_b32 s8, s2, 6
	v_or_b32_e32 v3, 0x600, v3
	v_add_u32_e32 v2, 0x780, v2
	v_cmp_gt_u32_e32 vcc, 16, v203
	s_ashr_i32 s6, s2, 7
	s_and_b32 s10, s8, 0x7c0
	v_lshrrev_b32_e32 v1, 5, v0
	v_cndmask_b32_e32 v3, v2, v3, vcc
	s_ashr_i32 s7, s6, 31
	v_lshl_or_b32 v2, v1, 2, s10
	v_lshlrev_b32_e32 v4, 1, v3
	v_mov_b32_e32 v5, v34
	s_lshl_b64 s[6:7], s[6:7], 11
	v_add_u32_e32 v6, -3, v2
	v_lshl_add_u64 v[4:5], s[58:59], 0, v[4:5]
	v_cmp_ne_u32_e32 vcc, 0, v2
	v_mov_b32_e32 v35, 0
	v_mov_b32_e32 v36, 0
	v_mov_b32_e32 v37, 0
	s_and_saveexec_b64 s[8:9], vcc
	s_cbranch_execz .LBB0_1777
	v_mov_b32_e32 v7, 0
	v_lshl_add_u64 v[8:9], s[6:7], 0, v[6:7]
	s_movk_i32 s14, 0x2600
	v_mad_u64_u32 v[10:11], s[12:13], v8, s14, v[4:5]
	v_mad_i32_i24 v11, v9, s14, v11
	global_load_dwordx4 v[34:37], v[10:11], off
